# speedup vs baseline: 1.0452x; 1.0033x over previous
.Lno_next:
	v_add_f32_e32 v2, v243, v2
	v_mov_b32_e32 v4, v2
	s_nop 1
	v_permlane32_swap_b32_e32 v2, v4
	v_add_f32_e32 v2, v2, v4
	v_div_scale_f32 v4, s[4:5], v2, v2, 1.0
	v_rcp_f32_e32 v5, v4
	v_mov_b32_e32 v6, v229
	v_fma_f32 v8, -v4, v5, 1.0
	v_fmac_f32_e32 v5, v8, v5
	v_div_scale_f32 v8, vcc, 1.0, v2, 1.0
	v_mul_f32_e32 v9, v8, v5
	v_fma_f32 v10, -v4, v9, v8
	v_fmac_f32_e32 v9, v10, v5
	v_fma_f32 v4, -v4, v9, v8
	v_div_fmas_f32 v4, v4, v5, v9
	v_lshlrev_b32_e32 v5, 8, v6
	v_ashrrev_i32_e32 v7, 5, v6
	v_and_b32_e32 v5, 0x1f00, v5
	v_div_fixup_f32 v2, v4, v2, 1.0
	v_add_u32_e32 v4, 8, v7
	v_add_u32_e32 v5, s84, v5
	v_bitop3_b32 v12, v7, v6, 15 bitop3:0x78
	v_pk_mul_f32 v[8:9], v[2:3], v[130:131] op_sel_hi:[0,1]
	v_pk_mul_f32 v[10:11], v[2:3], v[132:133] op_sel_hi:[0,1]
	v_lshl_add_u32 v12, v12, 4, v5
	v_bitop3_b32 v4, v4, v6, 15 bitop3:0x78
	ds_write_b128 v12, v[8:11]
	v_pk_mul_f32 v[8:9], v[2:3], v[114:115] op_sel_hi:[0,1]
	v_pk_mul_f32 v[10:11], v[2:3], v[116:117] op_sel_hi:[0,1]
	v_lshl_add_u32 v4, v4, 4, v5
	ds_write_b128 v4, v[8:11]
	v_add_u32_e32 v4, 2, v7
	v_bitop3_b32 v4, v4, v6, 15 bitop3:0x78
	v_add_u32_e32 v12, 10, v7
	v_pk_mul_f32 v[8:9], v[2:3], v[134:135] op_sel_hi:[0,1]
	v_pk_mul_f32 v[10:11], v[2:3], v[136:137] op_sel_hi:[0,1]
	v_lshl_add_u32 v4, v4, 4, v5
	ds_write_b128 v4, v[8:11]
	v_bitop3_b32 v4, v12, v6, 15 bitop3:0x78
	v_pk_mul_f32 v[8:9], v[2:3], v[118:119] op_sel_hi:[0,1]
	v_pk_mul_f32 v[10:11], v[2:3], v[120:121] op_sel_hi:[0,1]
	v_lshl_add_u32 v4, v4, 4, v5
	ds_write_b128 v4, v[8:11]
	v_add_u32_e32 v4, 4, v7
	v_bitop3_b32 v4, v4, v6, 15 bitop3:0x78
	v_add_u32_e32 v12, 12, v7
	v_pk_mul_f32 v[8:9], v[2:3], v[138:139] op_sel_hi:[0,1]
	v_pk_mul_f32 v[10:11], v[2:3], v[140:141] op_sel_hi:[0,1]
	v_lshl_add_u32 v4, v4, 4, v5
	ds_write_b128 v4, v[8:11]
	v_bitop3_b32 v4, v12, v6, 15 bitop3:0x78
	v_pk_mul_f32 v[8:9], v[2:3], v[122:123] op_sel_hi:[0,1]
	v_pk_mul_f32 v[10:11], v[2:3], v[124:125] op_sel_hi:[0,1]
	v_lshl_add_u32 v4, v4, 4, v5
	ds_write_b128 v4, v[8:11]
	v_add_u32_e32 v4, 6, v7
	v_bitop3_b32 v4, v4, v6, 15 bitop3:0x78
	v_add_u32_e32 v7, 14, v7
	v_pk_mul_f32 v[8:9], v[2:3], v[142:143] op_sel_hi:[0,1]
	v_pk_mul_f32 v[10:11], v[2:3], v[144:145] op_sel_hi:[0,1]
	v_lshl_add_u32 v4, v4, 4, v5
	ds_write_b128 v4, v[8:11]
	v_pk_mul_f32 v[8:9], v[2:3], v[126:127] op_sel_hi:[0,1]
	v_pk_mul_f32 v[10:11], v[2:3], v[128:129] op_sel_hi:[0,1]
	v_bitop3_b32 v2, v7, v6, 15 bitop3:0x78
	v_lshl_add_u32 v2, v2, 4, v5
	ds_write_b128 v2, v[8:11]
	v_ashrrev_i32_e32 v7, 4, v6
	v_lshlrev_b32_e32 v2, 2, v6
	v_and_or_b32 v2, v2, 60, s90
	v_lshl_add_u64 v[4:5], v[2:3], 2, s[72:73]
	v_mov_b32_e32 v8, v7
	v_xor_b32_e32 v9, v8, v6
	v_lshlrev_b32_e32 v9, 4, v9
	v_and_b32_e32 v9, 0xf0, v9
	v_lshlrev_b32_e32 v10, 8, v8
	v_add3_u32 v9, s84, v10, v9
	ds_read_b128 v[24:27], v9
	v_add_u32_e32 v8, 4, v7
	v_xor_b32_e32 v9, v8, v6
	v_lshlrev_b32_e32 v9, 4, v9
	v_and_b32_e32 v9, 0xf0, v9
	v_lshlrev_b32_e32 v10, 8, v8
	v_add3_u32 v9, s84, v10, v9
	ds_read_b128 v[28:31], v9
	v_add_u32_e32 v8, 8, v7
	v_xor_b32_e32 v9, v8, v6
	v_lshlrev_b32_e32 v9, 4, v9
	v_and_b32_e32 v9, 0xf0, v9
	v_lshlrev_b32_e32 v10, 8, v8
	v_add3_u32 v9, s84, v10, v9
	ds_read_b128 v[32:35], v9
	v_add_u32_e32 v8, 12, v7
	v_xor_b32_e32 v9, v8, v6
	v_lshlrev_b32_e32 v9, 4, v9
	v_and_b32_e32 v9, 0xf0, v9
	v_lshlrev_b32_e32 v10, 8, v8
	v_add3_u32 v9, s84, v10, v9
	ds_read_b128 v[36:39], v9
	v_add_u32_e32 v8, 16, v7
	v_xor_b32_e32 v9, v8, v6
	v_lshlrev_b32_e32 v9, 4, v9
	v_and_b32_e32 v9, 0xf0, v9
	v_lshlrev_b32_e32 v10, 8, v8
	v_add3_u32 v9, s84, v10, v9
	ds_read_b128 v[40:43], v9
	v_add_u32_e32 v8, 20, v7
	v_xor_b32_e32 v9, v8, v6
	v_lshlrev_b32_e32 v9, 4, v9
	v_and_b32_e32 v9, 0xf0, v9
	v_lshlrev_b32_e32 v10, 8, v8
	v_add3_u32 v9, s84, v10, v9
	ds_read_b128 v[44:47], v9
	v_add_u32_e32 v8, 24, v7
	v_xor_b32_e32 v9, v8, v6
	v_lshlrev_b32_e32 v9, 4, v9
	v_and_b32_e32 v9, 0xf0, v9
	v_lshlrev_b32_e32 v10, 8, v8
	v_add3_u32 v9, s84, v10, v9
	ds_read_b128 v[48:51], v9
	v_add_u32_e32 v8, 28, v7
	v_xor_b32_e32 v9, v8, v6
	v_lshlrev_b32_e32 v9, 4, v9
	v_and_b32_e32 v9, 0xf0, v9
	v_lshlrev_b32_e32 v10, 8, v8
	v_add3_u32 v9, s84, v10, v9
	ds_read_b128 v[52:55], v9
	v_add_u32_e32 v2, s88, v7
	v_cmp_gt_i32_e32 vcc, s3, v2
	v_add_lshl_u32 v2, v2, s76, 10
	v_lshl_add_u64 v[14:15], v[2:3], 2, v[4:5]
	s_and_saveexec_b64 s[4:5], vcc
	s_waitcnt lgkmcnt(7)
	global_store_dwordx4 v[14:15], v[24:27], off sc0 sc1
	s_or_b64 exec, exec, s[4:5]
	v_add_u32_e32 v8, 4, v7
	v_add_u32_e32 v2, s88, v8
	v_cmp_gt_i32_e32 vcc, s3, v2
	v_add_lshl_u32 v2, v2, s76, 10
	v_lshl_add_u64 v[14:15], v[2:3], 2, v[4:5]
	s_and_saveexec_b64 s[4:5], vcc
	s_waitcnt lgkmcnt(6)
	global_store_dwordx4 v[14:15], v[28:31], off sc0 sc1
	s_or_b64 exec, exec, s[4:5]
	v_add_u32_e32 v8, 8, v7
	v_add_u32_e32 v2, s88, v8
	v_cmp_gt_i32_e32 vcc, s3, v2
	v_add_lshl_u32 v2, v2, s76, 10
	v_lshl_add_u64 v[14:15], v[2:3], 2, v[4:5]
	s_and_saveexec_b64 s[4:5], vcc
	s_waitcnt lgkmcnt(5)
	global_store_dwordx4 v[14:15], v[32:35], off sc0 sc1
	s_or_b64 exec, exec, s[4:5]
	v_add_u32_e32 v8, 12, v7
	v_add_u32_e32 v2, s88, v8
	v_cmp_gt_i32_e32 vcc, s3, v2
	v_add_lshl_u32 v2, v2, s76, 10
	v_lshl_add_u64 v[14:15], v[2:3], 2, v[4:5]
	s_and_saveexec_b64 s[4:5], vcc
	s_waitcnt lgkmcnt(4)
	global_store_dwordx4 v[14:15], v[36:39], off sc0 sc1
	s_or_b64 exec, exec, s[4:5]
	v_add_u32_e32 v8, 16, v7
	v_add_u32_e32 v2, s88, v8
	v_cmp_gt_i32_e32 vcc, s3, v2
	v_add_lshl_u32 v2, v2, s76, 10
	v_lshl_add_u64 v[14:15], v[2:3], 2, v[4:5]
	s_and_saveexec_b64 s[4:5], vcc
	s_waitcnt lgkmcnt(3)
	global_store_dwordx4 v[14:15], v[40:43], off sc0 sc1
	s_or_b64 exec, exec, s[4:5]
	v_add_u32_e32 v8, 20, v7
	v_add_u32_e32 v2, s88, v8
	v_cmp_gt_i32_e32 vcc, s3, v2
	v_add_lshl_u32 v2, v2, s76, 10
	v_lshl_add_u64 v[14:15], v[2:3], 2, v[4:5]
	s_and_saveexec_b64 s[4:5], vcc
	s_waitcnt lgkmcnt(2)
	global_store_dwordx4 v[14:15], v[44:47], off sc0 sc1
	s_or_b64 exec, exec, s[4:5]
	v_add_u32_e32 v8, 24, v7
	v_add_u32_e32 v2, s88, v8
	v_cmp_gt_i32_e32 vcc, s3, v2
	v_add_lshl_u32 v2, v2, s76, 10
	v_lshl_add_u64 v[14:15], v[2:3], 2, v[4:5]
	s_and_saveexec_b64 s[4:5], vcc
	s_waitcnt lgkmcnt(1)
	global_store_dwordx4 v[14:15], v[48:51], off sc0 sc1
	s_or_b64 exec, exec, s[4:5]
	v_add_u32_e32 v8, 28, v7
	v_add_u32_e32 v2, s88, v8
	v_cmp_gt_i32_e32 vcc, s3, v2
	v_add_lshl_u32 v2, v2, s76, 10
	v_lshl_add_u64 v[14:15], v[2:3], 2, v[4:5]
	s_and_saveexec_b64 s[4:5], vcc
	s_waitcnt lgkmcnt(0)
	global_store_dwordx4 v[14:15], v[52:55], off sc0 sc1
	s_or_b64 exec, exec, s[4:5]
	s_branch .LBB0_4
